# speedup vs baseline: 1.0007x; 1.0007x over previous
_Z11init_kernelPKfS0_S0_S0_PDF16_S1_:
	s_load_dwordx8 s[4:11], s[0:1], 0x0
	s_load_dwordx4 s[12:15], s[0:1], 0x20
	v_readfirstlane_b32 s3, v0
	v_bfe_u32 v32, v0, 4, 2
	v_and_b32_e32 v33, 15, v0
	s_lshr_b32 s3, s3, 6
	s_lshl_b32 s17, s2, 11
	s_lshl_b32 s18, s2, 8
	s_lshl_b32 s19, s3, 7
	s_lshl_b32 s20, s3, 6
	v_mul_u32_u24_e32 v34, 36, v32
	v_lshl_or_b32 v34, v33, 7, v34
	v_mul_u32_u24_e32 v35, 0x900, v32
	v_lshl_or_b32 v35, v33, 3, v35
	v_lshlrev_b32_e32 v36, 3, v33
	v_lshlrev_b32_e32 v37, 4, v0
	v_lshlrev_b32_e32 v42, 9, v32
	v_lshl_or_b32 v42, v33, 2, v42
	v_mov_b32_e32 v44, 0
	v_mov_b32_e32 v45, 0
	v_mov_b32_e32 v46, 0
	v_mov_b32_e32 v47, 0
	v_mov_b32_e32 v39, 0
	v_mov_b32_e32 v41, 0
	v_add_u32_e32 v38, 20, v34
	v_lshlrev_b32_e32 v40, 4, v33
	v_cmp_eq_u32_e32 vcc, 3, v32
	s_waitcnt lgkmcnt(0)
	s_add_u32 s4, s4, s17
	s_addc_u32 s5, s5, 0
	s_add_u32 s6, s6, s18
	s_addc_u32 s7, s7, 0
	s_add_u32 s8, s8, s19
	s_addc_u32 s9, s9, 0
	v_lshl_add_u64 v[38:39], s[4:5], 0, v[38:39]
	v_lshl_add_u64 v[40:41], s[6:7], 0, v[40:41]
	v_cndmask_b32_e32 v38, v38, v40, vcc
	v_cndmask_b32_e32 v39, v39, v41, vcc
	global_load_dwordx4 v[2:5], v34, s[4:5] nt
	global_load_dword v6, v34, s[4:5] offset:16 nt
	global_load_dwordx4 v[8:11], v[38:39], off nt
	global_load_dwordx2 v[12:13], v35, s[8:9]
	global_load_dwordx2 v[14:15], v35, s[8:9] offset:256
	global_load_dwordx2 v[16:17], v35, s[8:9] offset:512
	global_load_dwordx2 v[18:19], v35, s[8:9] offset:768
	global_load_dwordx2 v[20:21], v35, s[8:9] offset:1024
	global_load_dwordx2 v[22:23], v35, s[8:9] offset:1280
	global_load_dwordx2 v[24:25], v35, s[8:9] offset:1536
	global_load_dwordx2 v[26:27], v35, s[8:9] offset:1792
	global_load_dwordx2 v[28:29], v35, s[8:9] offset:2048
	s_add_u32 s10, s10, s19
	s_addc_u32 s11, s11, 0
	global_load_dwordx2 v[30:31], v36, s[10:11]
	s_add_u32 s14, s14, s17
	s_addc_u32 s15, s15, 0
	s_add_u32 s12, s12, s17
	s_addc_u32 s13, s13, 0
	s_add_u32 s12, s12, s20
	s_addc_u32 s13, s13, 0
	global_store_dwordx4 v37, v[44:47], s[14:15]
	v_accvgpr_write_b32 a0, 0
	v_accvgpr_write_b32 a1, 0
	v_accvgpr_write_b32 a2, 0
	v_accvgpr_write_b32 a3, 0
	v_accvgpr_write_b32 a4, 0
	v_accvgpr_write_b32 a5, 0
	v_accvgpr_write_b32 a6, 0
	v_accvgpr_write_b32 a7, 0
	s_waitcnt vmcnt(11)
	s_waitcnt vmcnt(10)
	v_mfma_f32_16x16x4_f32 a[0:3], v2, v12, a[0:3]
	v_mfma_f32_16x16x4_f32 a[4:7], v2, v13, a[4:7]
	s_waitcnt vmcnt(9)
	v_mfma_f32_16x16x4_f32 a[0:3], v3, v14, a[0:3]
	v_mfma_f32_16x16x4_f32 a[4:7], v3, v15, a[4:7]
	s_waitcnt vmcnt(8)
	v_mfma_f32_16x16x4_f32 a[0:3], v4, v16, a[0:3]
	v_mfma_f32_16x16x4_f32 a[4:7], v4, v17, a[4:7]
	s_waitcnt vmcnt(7)
	v_mfma_f32_16x16x4_f32 a[0:3], v5, v18, a[0:3]
	v_mfma_f32_16x16x4_f32 a[4:7], v5, v19, a[4:7]
	s_waitcnt vmcnt(6)
	v_mfma_f32_16x16x4_f32 a[0:3], v6, v20, a[0:3]
	v_mfma_f32_16x16x4_f32 a[4:7], v6, v21, a[4:7]
	s_waitcnt vmcnt(5)
	v_mfma_f32_16x16x4_f32 a[0:3], v8, v22, a[0:3]
	v_mfma_f32_16x16x4_f32 a[4:7], v8, v23, a[4:7]
	s_waitcnt vmcnt(4)
	v_mfma_f32_16x16x4_f32 a[0:3], v9, v24, a[0:3]
	v_mfma_f32_16x16x4_f32 a[4:7], v9, v25, a[4:7]
	s_waitcnt vmcnt(3)
	v_mfma_f32_16x16x4_f32 a[0:3], v10, v26, a[0:3]
	v_mfma_f32_16x16x4_f32 a[4:7], v10, v27, a[4:7]
	s_waitcnt vmcnt(2)
	v_mfma_f32_16x16x4_f32 a[0:3], v11, v28, a[0:3]
	v_mfma_f32_16x16x4_f32 a[4:7], v11, v29, a[4:7]
	s_waitcnt vmcnt(1)
	s_nop 9
	v_accvgpr_read_b32 v2, a0
	v_accvgpr_read_b32 v3, a1
	v_accvgpr_read_b32 v4, a2
	v_accvgpr_read_b32 v5, a3
	v_accvgpr_read_b32 v6, a4
	v_accvgpr_read_b32 v7, a5
	v_accvgpr_read_b32 v8, a6
	v_accvgpr_read_b32 v9, a7
	v_add_f32_e32 v2, v30, v2
	v_add_f32_e32 v3, v30, v3
	v_add_f32_e32 v4, v30, v4
	v_add_f32_e32 v5, v30, v5
	v_add_f32_e32 v6, v31, v6
	v_add_f32_e32 v7, v31, v7
	v_add_f32_e32 v8, v31, v8
	v_add_f32_e32 v9, v31, v9
	v_cvt_pk_f16_f32 v2, v2, v6
	v_cvt_pk_f16_f32 v3, v3, v7
	v_cvt_pk_f16_f32 v4, v4, v8
	v_cvt_pk_f16_f32 v5, v5, v9
	global_store_dword v42, v2, s[12:13]
	global_store_dword v42, v3, s[12:13] offset:128
	global_store_dword v42, v4, s[12:13] offset:256
	global_store_dword v42, v5, s[12:13] offset:384
	s_endpgm
	.p2align	8

_Z12final_kernelPKDF16_S0_PKfS2_S2_S2_Pf:
	s_load_dwordx8 s[4:11], s[0:1], 0x0
	s_load_dwordx2 s[14:15], s[0:1], 0x20
	s_load_dwordx4 s[16:19], s[0:1], 0x28
	v_readfirstlane_b32 s3, v0
	v_bfe_u32 v70, v0, 4, 2
	v_and_b32_e32 v71, 15, v0
	s_lshr_b32 s3, s3, 6
	s_lshl_b32 s12, s2, 4
	s_lshl_b32 s20, s2, 11
	s_lshl_b32 s21, s3, 7
	s_lshl_b32 s22, s3, 6
	v_lshlrev_b32_e32 v72, 7, v71
	v_lshl_or_b32 v72, v70, 5, v72
	v_lshlrev_b32_e32 v73, 12, v70
	v_lshl_or_b32 v73, v71, 3, v73
	v_lshlrev_b32_e32 v74, 3, v71
	v_lshlrev_b32_e32 v75, 9, v70
	v_lshl_or_b32 v75, v71, 2, v75
	s_add_i32 s23, s22, 0x1080
	v_lshl_add_u32 v76, v70, 4, s23
	s_waitcnt lgkmcnt(0)
	s_load_dword s13, s[16:17], 0x0
	s_add_u32 s4, s4, s20
	s_addc_u32 s5, s5, 0
	s_add_u32 s8, s8, s21
	s_addc_u32 s9, s9, 0
	global_load_dwordx4 v[2:5], v72, s[4:5] nt
	global_load_dwordx4 v[6:9], v72, s[4:5] offset:16 nt
	global_load_dwordx2 v[26:27], v73, s[8:9]
	global_load_dwordx2 v[28:29], v73, s[8:9] offset:256
	global_load_dwordx2 v[30:31], v73, s[8:9] offset:512
	global_load_dwordx2 v[32:33], v73, s[8:9] offset:768
	global_load_dwordx2 v[34:35], v73, s[8:9] offset:1024
	global_load_dwordx2 v[36:37], v73, s[8:9] offset:1280
	global_load_dwordx2 v[38:39], v73, s[8:9] offset:1536
	global_load_dwordx2 v[40:41], v73, s[8:9] offset:1792
	global_load_dwordx2 v[42:43], v73, s[8:9] offset:2048
	global_load_dwordx2 v[44:45], v73, s[8:9] offset:2304
	global_load_dwordx2 v[46:47], v73, s[8:9] offset:2560
	global_load_dwordx2 v[48:49], v73, s[8:9] offset:2816
	global_load_dwordx2 v[50:51], v73, s[8:9] offset:3072
	global_load_dwordx2 v[52:53], v73, s[8:9] offset:3328
	global_load_dwordx2 v[54:55], v73, s[8:9] offset:3584
	global_load_dwordx2 v[56:57], v73, s[8:9] offset:3840
	s_add_u32 s6, s6, s20
	s_addc_u32 s7, s7, 0
	s_add_u32 s6, s6, s22
	s_addc_u32 s7, s7, 0
	global_load_dword v60, v75, s[6:7] nt
	global_load_dword v61, v75, s[6:7] offset:128 nt
	global_load_dword v62, v75, s[6:7] offset:256 nt
	global_load_dword v63, v75, s[6:7] offset:384 nt
	s_add_u32 s10, s10, s21
	s_addc_u32 s11, s11, 0
	global_load_dwordx2 v[58:59], v74, s[10:11]
	s_add_u32 s14, s14, s21
	s_addc_u32 s15, s15, 0
	global_load_dwordx2 v[68:69], v74, s[14:15]
	v_accvgpr_write_b32 a0, 0
	v_accvgpr_write_b32 a1, 0
	v_accvgpr_write_b32 a2, 0
	v_accvgpr_write_b32 a3, 0
	v_accvgpr_write_b32 a4, 0
	v_accvgpr_write_b32 a5, 0
	v_accvgpr_write_b32 a6, 0
	v_accvgpr_write_b32 a7, 0
	s_waitcnt vmcnt(22)
	v_cvt_f32_f16_e32 v10, v2
	v_cvt_f32_f16_sdwa v11, v2 dst_sel:DWORD dst_unused:UNUSED_PAD src0_sel:WORD_1
	v_cvt_f32_f16_e32 v12, v3
	v_cvt_f32_f16_sdwa v13, v3 dst_sel:DWORD dst_unused:UNUSED_PAD src0_sel:WORD_1
	v_cvt_f32_f16_e32 v14, v4
	v_cvt_f32_f16_sdwa v15, v4 dst_sel:DWORD dst_unused:UNUSED_PAD src0_sel:WORD_1
	v_cvt_f32_f16_e32 v16, v5
	v_cvt_f32_f16_sdwa v17, v5 dst_sel:DWORD dst_unused:UNUSED_PAD src0_sel:WORD_1
	v_cvt_f32_f16_e32 v18, v6
	v_cvt_f32_f16_sdwa v19, v6 dst_sel:DWORD dst_unused:UNUSED_PAD src0_sel:WORD_1
	v_cvt_f32_f16_e32 v20, v7
	v_cvt_f32_f16_sdwa v21, v7 dst_sel:DWORD dst_unused:UNUSED_PAD src0_sel:WORD_1
	v_cvt_f32_f16_e32 v22, v8
	v_cvt_f32_f16_sdwa v23, v8 dst_sel:DWORD dst_unused:UNUSED_PAD src0_sel:WORD_1
	v_cvt_f32_f16_e32 v24, v9
	v_cvt_f32_f16_sdwa v25, v9 dst_sel:DWORD dst_unused:UNUSED_PAD src0_sel:WORD_1
	v_max_f32_e32 v10, 0, v10
	v_max_f32_e32 v11, 0, v11
	v_max_f32_e32 v12, 0, v12
	v_max_f32_e32 v13, 0, v13
	v_max_f32_e32 v14, 0, v14
	v_max_f32_e32 v15, 0, v15
	v_max_f32_e32 v16, 0, v16
	v_max_f32_e32 v17, 0, v17
	v_max_f32_e32 v18, 0, v18
	v_max_f32_e32 v19, 0, v19
	v_max_f32_e32 v20, 0, v20
	v_max_f32_e32 v21, 0, v21
	v_max_f32_e32 v22, 0, v22
	v_max_f32_e32 v23, 0, v23
	v_max_f32_e32 v24, 0, v24
	v_max_f32_e32 v25, 0, v25
	s_waitcnt vmcnt(21)
	v_mfma_f32_16x16x4_f32 a[0:3], v10, v26, a[0:3]
	v_mfma_f32_16x16x4_f32 a[4:7], v10, v27, a[4:7]
	s_waitcnt vmcnt(20)
	v_mfma_f32_16x16x4_f32 a[0:3], v11, v28, a[0:3]
	v_mfma_f32_16x16x4_f32 a[4:7], v11, v29, a[4:7]
	s_waitcnt vmcnt(19)
	v_mfma_f32_16x16x4_f32 a[0:3], v12, v30, a[0:3]
	v_mfma_f32_16x16x4_f32 a[4:7], v12, v31, a[4:7]
	s_waitcnt vmcnt(18)
	v_mfma_f32_16x16x4_f32 a[0:3], v13, v32, a[0:3]
	v_mfma_f32_16x16x4_f32 a[4:7], v13, v33, a[4:7]
	s_waitcnt vmcnt(17)
	v_mfma_f32_16x16x4_f32 a[0:3], v14, v34, a[0:3]
	v_mfma_f32_16x16x4_f32 a[4:7], v14, v35, a[4:7]
	s_waitcnt vmcnt(16)
	v_mfma_f32_16x16x4_f32 a[0:3], v15, v36, a[0:3]
	v_mfma_f32_16x16x4_f32 a[4:7], v15, v37, a[4:7]
	s_waitcnt vmcnt(15)
	v_mfma_f32_16x16x4_f32 a[0:3], v16, v38, a[0:3]
	v_mfma_f32_16x16x4_f32 a[4:7], v16, v39, a[4:7]
	s_waitcnt vmcnt(14)
	v_mfma_f32_16x16x4_f32 a[0:3], v17, v40, a[0:3]
	v_mfma_f32_16x16x4_f32 a[4:7], v17, v41, a[4:7]
	s_waitcnt vmcnt(13)
	v_mfma_f32_16x16x4_f32 a[0:3], v18, v42, a[0:3]
	v_mfma_f32_16x16x4_f32 a[4:7], v18, v43, a[4:7]
	s_waitcnt vmcnt(12)
	v_mfma_f32_16x16x4_f32 a[0:3], v19, v44, a[0:3]
	v_mfma_f32_16x16x4_f32 a[4:7], v19, v45, a[4:7]
	s_waitcnt vmcnt(11)
	v_mfma_f32_16x16x4_f32 a[0:3], v20, v46, a[0:3]
	v_mfma_f32_16x16x4_f32 a[4:7], v20, v47, a[4:7]
	s_waitcnt vmcnt(10)
	v_mfma_f32_16x16x4_f32 a[0:3], v21, v48, a[0:3]
	v_mfma_f32_16x16x4_f32 a[4:7], v21, v49, a[4:7]
	s_waitcnt vmcnt(9)
	v_mfma_f32_16x16x4_f32 a[0:3], v22, v50, a[0:3]
	v_mfma_f32_16x16x4_f32 a[4:7], v22, v51, a[4:7]
	s_waitcnt vmcnt(8)
	v_mfma_f32_16x16x4_f32 a[0:3], v23, v52, a[0:3]
	v_mfma_f32_16x16x4_f32 a[4:7], v23, v53, a[4:7]
	s_waitcnt vmcnt(7)
	v_mfma_f32_16x16x4_f32 a[0:3], v24, v54, a[0:3]
	v_mfma_f32_16x16x4_f32 a[4:7], v24, v55, a[4:7]
	s_waitcnt vmcnt(6)
	v_mfma_f32_16x16x4_f32 a[0:3], v25, v56, a[0:3]
	v_mfma_f32_16x16x4_f32 a[4:7], v25, v57, a[4:7]
	v_cmp_eq_u32_e32 vcc, 0, v71
	s_waitcnt vmcnt(0)
	v_cvt_f32_f16_sdwa v64, v60 dst_sel:DWORD dst_unused:UNUSED_PAD src0_sel:WORD_1
	v_cvt_f32_f16_sdwa v65, v61 dst_sel:DWORD dst_unused:UNUSED_PAD src0_sel:WORD_1
	v_cvt_f32_f16_sdwa v66, v62 dst_sel:DWORD dst_unused:UNUSED_PAD src0_sel:WORD_1
	v_cvt_f32_f16_sdwa v67, v63 dst_sel:DWORD dst_unused:UNUSED_PAD src0_sel:WORD_1
	v_cvt_f32_f16_e32 v60, v60
	v_cvt_f32_f16_e32 v61, v61
	v_cvt_f32_f16_e32 v62, v62
	v_cvt_f32_f16_e32 v63, v63
	v_add_f32_e32 v60, v58, v60
	v_add_f32_e32 v64, v59, v64
	v_add_f32_e32 v61, v58, v61
	v_add_f32_e32 v65, v59, v65
	v_add_f32_e32 v62, v58, v62
	v_add_f32_e32 v66, v59, v66
	v_add_f32_e32 v63, v58, v63
	v_add_f32_e32 v67, v59, v67
	s_nop 1
	v_accvgpr_read_b32 v2, a0
	v_accvgpr_read_b32 v3, a1
	v_accvgpr_read_b32 v4, a2
	v_accvgpr_read_b32 v5, a3
	v_accvgpr_read_b32 v6, a4
	v_accvgpr_read_b32 v7, a5
	v_accvgpr_read_b32 v8, a6
	v_accvgpr_read_b32 v9, a7
	v_add_f32_e32 v2, v2, v60
	v_add_f32_e32 v3, v3, v61
	v_add_f32_e32 v4, v4, v62
	v_add_f32_e32 v5, v5, v63
	v_add_f32_e32 v6, v6, v64
	v_add_f32_e32 v7, v7, v65
	v_add_f32_e32 v8, v8, v66
	v_add_f32_e32 v9, v9, v67
	v_max_f32_e32 v2, 0, v2
	v_max_f32_e32 v3, 0, v3
	v_max_f32_e32 v4, 0, v4
	v_max_f32_e32 v5, 0, v5
	v_max_f32_e32 v6, 0, v6
	v_max_f32_e32 v7, 0, v7
	v_max_f32_e32 v8, 0, v8
	v_max_f32_e32 v9, 0, v9
	v_mul_f32_e32 v6, v69, v6
	v_mul_f32_e32 v7, v69, v7
	v_mul_f32_e32 v8, v69, v8
	v_mul_f32_e32 v9, v69, v9
	v_fmac_f32_e32 v6, v68, v2
	v_fmac_f32_e32 v7, v68, v3
	v_fmac_f32_e32 v8, v68, v4
	v_fmac_f32_e32 v9, v68, v5
	v_add_f32_dpp v6, v6, v6 quad_perm:[1,0,3,2] row_mask:0xf bank_mask:0xf
	v_add_f32_dpp v7, v7, v7 quad_perm:[1,0,3,2] row_mask:0xf bank_mask:0xf
	v_add_f32_dpp v8, v8, v8 quad_perm:[1,0,3,2] row_mask:0xf bank_mask:0xf
	v_add_f32_dpp v9, v9, v9 quad_perm:[1,0,3,2] row_mask:0xf bank_mask:0xf
	v_add_f32_dpp v6, v6, v6 quad_perm:[2,3,0,1] row_mask:0xf bank_mask:0xf
	v_add_f32_dpp v7, v7, v7 quad_perm:[2,3,0,1] row_mask:0xf bank_mask:0xf
	v_add_f32_dpp v8, v8, v8 quad_perm:[2,3,0,1] row_mask:0xf bank_mask:0xf
	v_add_f32_dpp v9, v9, v9 quad_perm:[2,3,0,1] row_mask:0xf bank_mask:0xf
	v_add_f32_dpp v6, v6, v6 row_half_mirror row_mask:0xf bank_mask:0xf
	v_add_f32_dpp v7, v7, v7 row_half_mirror row_mask:0xf bank_mask:0xf
	v_add_f32_dpp v8, v8, v8 row_half_mirror row_mask:0xf bank_mask:0xf
	v_add_f32_dpp v9, v9, v9 row_half_mirror row_mask:0xf bank_mask:0xf
	v_add_f32_dpp v6, v6, v6 row_mirror row_mask:0xf bank_mask:0xf
	v_add_f32_dpp v7, v7, v7 row_mirror row_mask:0xf bank_mask:0xf
	v_add_f32_dpp v8, v8, v8 row_mirror row_mask:0xf bank_mask:0xf
	v_add_f32_dpp v9, v9, v9 row_mirror row_mask:0xf bank_mask:0xf
	s_and_saveexec_b64 s[2:3], vcc
	ds_write_b128 v76, v[6:9]
	s_or_b64 exec, exec, s[2:3]
	v_cmp_gt_u32_e32 vcc, 16, v0
	s_waitcnt lgkmcnt(0)
	s_barrier
	s_and_saveexec_b64 s[2:3], vcc
	s_cbranch_execz .Lfinal_done
	v_lshlrev_b32_e32 v1, 2, v0
	v_add_u32_e32 v1, 0x1000, v1
	ds_read2_b32 v[2:3], v1 offset0:32 offset1:48
	v_or_b32_e32 v0, s12, v0
	v_ashrrev_i32_e32 v1, 31, v0
	v_lshl_add_u64 v[0:1], v[0:1], 2, s[18:19]
	s_waitcnt lgkmcnt(0)
	v_add_f32_e32 v2, v2, v3
	v_add_f32_e32 v2, s13, v2
	global_store_dword v[0:1], v2, off
